# v55 + RG-LRU phases: stagger of the backward wave half tripled (s_sleep 24 instead of 8)
# baseline (speedup 1.0000x reference)
; #define LAS __attribute__((address_space(3)))
; __device__ __forceinline__ int crow(int r, int hh) { return (r & 3) + 8 * (r >> 2) + 4 * hh; }
; template <bool FINAL, int z> __device__ __forceinline__ void rglru_blocks(LAS unsigned char* XCB, LAS float* XCF, LAS float* HS, const bf16x8 (&wa)[8], const bf16x8 (&wx)[8],
;         float ba, float bxx, float sp8, int r, int hh, int chl, float& st, float& CA, float& CB) {
;     ...
;         for (int bi = 0; bi < 2; ++bi) { const int tb = z ? 1 - bi : bi;
;             if (z == 1 && bi == 0) __builtin_amdgcn_s_sleep(8);
;             f32x16 ya, yx;
; #pragma unroll
;             for (int i = 0; i < 16; ++i) { ya[i] = ba; yx[i] = bxx; }
; #pragma unroll
;             for (int s = 0; s < 8; ++s) { const bf16x8 af = *(const LAS bf16x8*)(XCB + (32 * tb + r) * 272 + (16 * s + 8 * hh) * 2);
;                 ya = __builtin_amdgcn_mfma_f32_32x32x16_bf16(af, wa[s], ya, 0, 0, 0); yx = __builtin_amdgcn_mfma_f32_32x32x16_bf16(af, wx[s], yx, 0, 0, 0); }
;             float av[16], bv[16];
; #pragma unroll
;             for (int i = 0; i < 16; i += 2) {
;                 typedef float f2 __attribute__((ext_vector_type(2)));
;                 const f2 xc = {XCF[(32 * tb + crow(i, hh)) * 128 + chl], XCF[(32 * tb + crow(i + 1, hh)) * 128 + chl]};
;                 const f2 ta = (f2){ya[i], ya[i + 1]} * -1.4426950408889634f, tx = (f2){yx[i], yx[i + 1]} * -1.4426950408889634f;
;                 f2 ea, ex; ea.x = __builtin_amdgcn_exp2f(ta.x); ea.y = __builtin_amdgcn_exp2f(ta.y); ex.x = __builtin_amdgcn_exp2f(tx.x); ex.y = __builtin_amdgcn_exp2f(tx.y);
;                 const f2 da = ea + 1.0f, dx = ex + 1.0f;
;                 f2 rg, ig; rg.x = __builtin_amdgcn_rcpf(da.x); rg.y = __builtin_amdgcn_rcpf(da.y); ig.x = __builtin_amdgcn_rcpf(dx.x); ig.y = __builtin_amdgcn_rcpf(dx.y);
;                 const f2 la = rg * sp8; f2 a; a.x = __builtin_amdgcn_exp2f(la.x); a.y = __builtin_amdgcn_exp2f(la.y);
;                 const f2 om = a * -a + 1.0f; f2 sq; sq.x = __builtin_amdgcn_sqrtf(om.x); sq.y = __builtin_amdgcn_sqrtf(om.y);
;                 const f2 b = sq * ig * xc;
;                 av[i] = a.x; av[i + 1] = a.y; bv[i] = b.x; bv[i + 1] = b.y; }
.LBB0_1410:
	v_and_b32_e32 v35, 64, v184
	v_xor_b32_e32 v34, 32, v184
	v_add_u32_e32 v35, 64, v35
	v_cmp_lt_i32_e32 vcc, v34, v35
	s_mov_b64 s[6:7], -1
	s_nop 0
	v_cndmask_b32_e32 v34, v184, v34, vcc
	v_lshlrev_b32_e32 v155, 2, v34
	s_and_b64 vcc, exec, s[16:17]
	s_cbranch_vccz .LBB0_1441
	s_sleep 24
	ds_read_b128 v[170:173], v185 offset:8704
	ds_read_b128 v[188:191], v185 offset:8736
	s_waitcnt lgkmcnt(1)
	v_mfma_f32_32x32x16_bf16 v[50:65], v[170:173], v[66:69], v[2:17]
	v_mfma_f32_32x32x16_bf16 v[34:49], v[170:173], v[98:101], v[18:33]
	s_waitcnt lgkmcnt(0)
	v_mfma_f32_32x32x16_bf16 v[50:65], v[188:191], v[70:73], v[50:65]
	v_mfma_f32_32x32x16_bf16 v[34:49], v[188:191], v[102:105], v[34:49]
	ds_read_b128 v[170:173], v185 offset:8768
	ds_read_b128 v[188:191], v185 offset:8800
	s_waitcnt lgkmcnt(1)
	v_mfma_f32_32x32x16_bf16 v[50:65], v[170:173], v[74:77], v[50:65]
	v_mfma_f32_32x32x16_bf16 v[34:49], v[170:173], v[106:109], v[34:49]
	s_waitcnt lgkmcnt(0)
	v_mfma_f32_32x32x16_bf16 v[50:65], v[188:191], v[78:81], v[50:65]
	v_mfma_f32_32x32x16_bf16 v[34:49], v[188:191], v[110:113], v[34:49]
	ds_read_b128 v[170:173], v185 offset:8832
	ds_read_b128 v[188:191], v185 offset:8864
	s_waitcnt lgkmcnt(1)
	v_mfma_f32_32x32x16_bf16 v[50:65], v[170:173], v[82:85], v[50:65]
	v_mfma_f32_32x32x16_bf16 v[34:49], v[170:173], v[114:117], v[34:49]
	s_waitcnt lgkmcnt(0)
	v_mfma_f32_32x32x16_bf16 v[50:65], v[188:191], v[86:89], v[50:65]
	v_mfma_f32_32x32x16_bf16 v[34:49], v[188:191], v[118:121], v[34:49]
	ds_read_b128 v[170:173], v185 offset:8896
	ds_read_b128 v[188:191], v185 offset:8928
	ds_read2st64_b32 v[192:193], v186 offset0:168 offset1:170
	ds_read2st64_b32 v[196:197], v186 offset0:180 offset1:182
	s_waitcnt lgkmcnt(3)
	v_mfma_f32_32x32x16_bf16 v[50:65], v[170:173], v[90:93], v[50:65]
	s_waitcnt lgkmcnt(2)
	v_mfma_f32_32x32x16_bf16 v[50:65], v[188:191], v[94:97], v[50:65]
	v_mfma_f32_32x32x16_bf16 v[34:49], v[170:173], v[122:125], v[34:49]
	s_nop 10
	v_mul_f32_e64 v50, v50, s20
	v_mul_f32_e64 v51, v51, s20
	v_mul_f32_e64 v56, v56, s20
	v_mul_f32_e64 v57, v57, s20
	v_exp_f32_e32 v50, v50
	v_exp_f32_e32 v51, v51
	v_exp_f32_e32 v56, v56
	v_exp_f32_e32 v57, v57
	v_pk_mul_f32 v[54:55], v[54:55], s[20:21] op_sel_hi:[1,0]
	v_pk_add_f32 v[50:51], v[50:51], 1.0 op_sel_hi:[1,0]
	v_mfma_f32_32x32x16_bf16 v[34:49], v[188:191], v[126:129], v[34:49]
	v_rcp_f32_e32 v172, v50
	v_rcp_f32_e32 v173, v51
	v_pk_mul_f32 v[50:51], v[52:53], s[20:21] op_sel_hi:[1,0]
	v_pk_add_f32 v[56:57], v[56:57], 1.0 op_sel_hi:[1,0]
	v_exp_f32_e32 v52, v50
	v_exp_f32_e32 v53, v51
	v_rcp_f32_e32 v56, v56
	s_nop 4
	v_pk_mul_f32 v[34:35], v[34:35], s[20:21] op_sel_hi:[1,0]
	v_pk_mul_f32 v[36:37], v[36:37], s[20:21] op_sel_hi:[1,0]
	v_pk_add_f32 v[52:53], v[52:53], 1.0 op_sel_hi:[1,0]
	v_exp_f32_e32 v170, v34
	v_rcp_f32_e32 v52, v52
	v_rcp_f32_e32 v53, v53
	v_exp_f32_e32 v171, v35
	v_exp_f32_e32 v36, v36
	v_exp_f32_e32 v37, v37
	v_pk_mul_f32 v[52:53], v[164:165], v[52:53]
	v_pk_add_f32 v[170:171], v[170:171], 1.0 op_sel_hi:[1,0]
	v_exp_f32_e32 v52, v52
	v_exp_f32_e32 v53, v53
	v_pk_add_f32 v[36:37], v[36:37], 1.0 op_sel_hi:[1,0]
	v_rcp_f32_e32 v50, v170
	v_rcp_f32_e32 v51, v171
	v_pk_mul_f32 v[170:171], v[164:165], v[172:173]
	v_rcp_f32_e32 v172, v36
	v_rcp_f32_e32 v173, v37
	v_pk_fma_f32 v[36:37], v[52:53], v[52:53], 1.0 op_sel_hi:[1,1,0] neg_lo:[1,0,0] neg_hi:[1,0,0]
	v_rcp_f32_e32 v57, v57
	v_sqrt_f32_e32 v174, v36
	v_sqrt_f32_e32 v175, v37
	v_exp_f32_e32 v36, v170
	v_exp_f32_e32 v37, v171
	ds_read2st64_b32 v[170:171], v186 offset0:136 offset1:138
	v_pk_mul_f32 v[38:39], v[38:39], s[20:21] op_sel_hi:[1,0]
	v_pk_mul_f32 v[40:41], v[40:41], s[20:21] op_sel_hi:[1,0]
	v_pk_mul_f32 v[56:57], v[164:165], v[56:57]
	v_pk_mul_f32 v[172:173], v[172:173], v[174:175]
	v_exp_f32_e32 v174, v54
	v_exp_f32_e32 v175, v55
	v_exp_f32_e32 v38, v38
	v_exp_f32_e32 v39, v39
	v_exp_f32_e32 v40, v40
	v_exp_f32_e32 v41, v41
	v_exp_f32_e32 v56, v56
	v_exp_f32_e32 v57, v57
	s_waitcnt lgkmcnt(0)
	v_pk_mul_f32 v[170:171], v[170:171], v[172:173]
	v_pk_add_f32 v[172:173], v[174:175], 1.0 op_sel_hi:[1,0]
	v_pk_add_f32 v[38:39], v[38:39], 1.0 op_sel_hi:[1,0]
	v_pk_add_f32 v[40:41], v[40:41], 1.0 op_sel_hi:[1,0]
	v_pk_fma_f32 v[188:189], v[56:57], v[56:57], 1.0 op_sel_hi:[1,1,0] neg_lo:[1,0,0] neg_hi:[1,0,0]
	v_rcp_f32_e32 v172, v172
	v_rcp_f32_e32 v173, v173
	v_rcp_f32_e32 v174, v38
	v_rcp_f32_e32 v175, v39
	ds_read2st64_b32 v[38:39], v186 offset0:152 offset1:154
	v_rcp_f32_e32 v40, v40
	v_rcp_f32_e32 v41, v41
	v_sqrt_f32_e32 v188, v188
	v_sqrt_f32_e32 v189, v189
	v_pk_mul_f32 v[172:173], v[164:165], v[172:173]
	ds_read2st64_b32 v[34:35], v186 offset0:132 offset1:134
	v_exp_f32_e32 v191, v172
	v_pk_mul_f32 v[40:41], v[40:41], v[188:189]
	v_exp_f32_e32 v190, v173
	s_waitcnt lgkmcnt(1)
; template <bool FINAL, int z> __device__ __forceinline__ void rglru_blocks(LAS unsigned char* XCB, LAS float* XCF, LAS float* HS, const bf16x8 (&wa)[8], const bf16x8 (&wx)[8],
;         float ba, float bxx, float sp8, int r, int hh, int chl, float& st, float& CA, float& CB) {
;     ...
;                 const f2 ta = (f2){ya[i], ya[i + 1]} * -1.4426950408889634f, tx = (f2){yx[i], yx[i + 1]} * -1.4426950408889634f;
;                 f2 ea, ex; ea.x = __builtin_amdgcn_exp2f(ta.x); ea.y = __builtin_amdgcn_exp2f(ta.y); ex.x = __builtin_amdgcn_exp2f(tx.x); ex.y = __builtin_amdgcn_exp2f(tx.y);
;                 const f2 da = ea + 1.0f, dx = ex + 1.0f;
;                 f2 rg, ig; rg.x = __builtin_amdgcn_rcpf(da.x); rg.y = __builtin_amdgcn_rcpf(da.y); ig.x = __builtin_amdgcn_rcpf(dx.x); ig.y = __builtin_amdgcn_rcpf(dx.y);
;                 const f2 la = rg * sp8; f2 a; a.x = __builtin_amdgcn_exp2f(la.x); a.y = __builtin_amdgcn_exp2f(la.y);
;                 const f2 om = a * -a + 1.0f; f2 sq; sq.x = __builtin_amdgcn_sqrtf(om.x); sq.y = __builtin_amdgcn_sqrtf(om.y);
;                 const f2 b = sq * ig * xc;
;                 av[i] = a.x; av[i + 1] = a.y; bv[i] = b.x; bv[i + 1] = b.y; }
;             float Ag[4], Bg[4], Ap[4], Bp[4];
; #pragma unroll
;             for (int g = 0; g < 4; ++g) { float A = 1.f, B = 0.f;
; #pragma unroll
;                 for (int k = 0; k < 4; ++k) { const int kk = z ? 3 - k : k; B = B * av[4 * g + kk] + bv[4 * g + kk]; A *= av[4 * g + kk]; }
;                 Ag[g] = A; Bg[g] = B; Ap[g] = __shfl_xor(A, 32); Bp[g] = __shfl_xor(B, 32); }
;             float ent[4]; float cur = st;
; #pragma unroll
;             for (int gi = 0; gi < 4; ++gi) { const int g = z ? 3 - gi : gi;
;                 const bool own_first = z ? (hh == 1) : (hh == 0);
;                 if (own_first) { ent[g] = cur; cur = Ag[g] * cur + Bg[g]; CB = Ag[g] * CB + Bg[g]; CA *= Ag[g]; cur = Ap[g] * cur + Bp[g]; CB = Ap[g] * CB + Bp[g]; CA *= Ap[g]; }
;                 else { cur = Ap[g] * cur + Bp[g]; CB = Ap[g] * CB + Bp[g]; CA *= Ap[g]; ent[g] = cur; cur = Ag[g] * cur + Bg[g]; CB = Ag[g] * CB + Bg[g]; CA *= Ag[g]; } }
	v_pk_mul_f32 v[172:173], v[38:39], v[40:41]
	v_pk_mul_f32 v[38:39], v[58:59], s[20:21] op_sel_hi:[1,0]
	v_pk_mul_f32 v[40:41], v[42:43], s[20:21] op_sel_hi:[1,0]
	v_exp_f32_e32 v38, v38
	v_exp_f32_e32 v39, v39
	v_exp_f32_e32 v40, v40
	v_exp_f32_e32 v41, v41
	v_pk_mul_f32 v[42:43], v[44:45], s[20:21] op_sel_hi:[1,0]
	v_pk_add_f32 v[38:39], v[38:39], 1.0 op_sel_hi:[1,0]
	v_exp_f32_e32 v42, v42
	v_rcp_f32_e32 v38, v38
	v_rcp_f32_e32 v39, v39
	v_pk_add_f32 v[40:41], v[40:41], 1.0 op_sel_hi:[1,0]
	v_exp_f32_e32 v43, v43
	v_rcp_f32_e32 v58, v40
	v_rcp_f32_e32 v59, v41
	v_pk_mul_f32 v[40:41], v[164:165], v[38:39]
	v_pk_add_f32 v[42:43], v[42:43], 1.0 op_sel_hi:[1,0]
	v_exp_f32_e32 v39, v40
	v_exp_f32_e32 v38, v41
	v_pk_mul_f32 v[40:41], v[60:61], s[20:21] op_sel_hi:[1,0]
	v_rcp_f32_e32 v60, v42
	v_exp_f32_e32 v40, v40
	v_exp_f32_e32 v41, v41
	v_rcp_f32_e32 v61, v43
	v_pk_mul_f32 v[42:43], v[62:63], s[20:21] op_sel_hi:[1,0]
	v_pk_mul_f32 v[44:45], v[46:47], s[20:21] op_sel_hi:[1,0]
	v_pk_add_f32 v[40:41], v[40:41], 1.0 op_sel_hi:[1,0]
	v_exp_f32_e32 v42, v42
	v_rcp_f32_e32 v40, v40
	v_rcp_f32_e32 v41, v41
	v_exp_f32_e32 v43, v43
	v_exp_f32_e32 v44, v44
	v_exp_f32_e32 v45, v45
	v_pk_mul_f32 v[40:41], v[164:165], v[40:41]
	v_pk_mul_f32 v[46:47], v[48:49], s[20:21] op_sel_hi:[1,0]
	v_exp_f32_e32 v194, v40
	v_exp_f32_e32 v63, v41
	v_pk_add_f32 v[40:41], v[42:43], 1.0 op_sel_hi:[1,0]
	v_pk_add_f32 v[42:43], v[44:45], 1.0 op_sel_hi:[1,0]
	v_pk_mul_f32 v[44:45], v[64:65], s[20:21] op_sel_hi:[1,0]
	v_exp_f32_e32 v46, v46
	v_exp_f32_e32 v44, v44
	v_exp_f32_e32 v45, v45
	v_exp_f32_e32 v47, v47
	v_rcp_f32_e32 v40, v40
	v_rcp_f32_e32 v41, v41
	v_pk_add_f32 v[44:45], v[44:45], 1.0 op_sel_hi:[1,0]
	v_rcp_f32_e32 v64, v42
	v_rcp_f32_e32 v44, v44
	v_rcp_f32_e32 v45, v45
	v_rcp_f32_e32 v65, v43
	ds_read2st64_b32 v[42:43], v186 offset0:184 offset1:186
	v_pk_mul_f32 v[40:41], v[164:165], v[40:41]
	v_pk_mul_f32 v[44:45], v[164:165], v[44:45]
	v_exp_f32_e32 v198, v40
	v_exp_f32_e32 v48, v44
	v_exp_f32_e32 v49, v45
	v_pk_add_f32 v[44:45], v[46:47], 1.0 op_sel_hi:[1,0]
	v_exp_f32_e32 v62, v41
	v_rcp_f32_e32 v44, v44
	v_pk_fma_f32 v[46:47], v[48:49], v[48:49], 1.0 op_sel_hi:[1,1,0] neg_lo:[1,0,0] neg_hi:[1,0,0]
	v_rcp_f32_e32 v45, v45
	v_sqrt_f32_e32 v46, v46
	v_sqrt_f32_e32 v47, v47
	ds_read2st64_b32 v[54:55], v186 offset0:148 offset1:150
	v_mov_b32_e32 v195, v63
	ds_read2st64_b32 v[188:189], v186 offset0:164 offset1:166
	v_pk_mul_f32 v[40:41], v[44:45], v[46:47]
	v_mov_b32_e32 v199, v38
	s_waitcnt lgkmcnt(2)
	v_pk_mul_f32 v[200:201], v[42:43], v[40:41]
	v_pk_fma_f32 v[40:41], v[36:37], v[36:37], 1.0 op_sel_hi:[1,1,0] neg_lo:[1,0,0] neg_hi:[1,0,0]
	v_fma_f32 v42, 0, v53, v171
	v_sqrt_f32_e32 v40, v40
	v_sqrt_f32_e32 v41, v41
	v_fmac_f32_e32 v170, v52, v42
	v_mul_f32_e32 v43, v53, v52
	v_pk_mul_f32 v[40:41], v[50:51], v[40:41]
	s_nop 0
	v_pk_mul_f32 v[40:41], v[34:35], v[40:41]
	s_nop 0
	v_fma_f32 v42, v37, v170, v41
	v_mov_b32_e32 v41, v36
	v_pk_mul_f32 v[44:45], v[36:37], v[42:43]
	v_pk_fma_f32 v[34:35], v[36:37], v[42:43], v[40:41]
	v_pk_fma_f32 v[42:43], v[190:191], v[190:191], 1.0 op_sel_hi:[1,1,0] neg_lo:[1,0,0] neg_hi:[1,0,0]
	v_pk_mul_f32 v[40:41], v[40:41], v[44:45]
	v_sqrt_f32_e32 v44, v43
	v_sqrt_f32_e32 v45, v42
	v_fma_f32 v35, 0, v57, v173
	v_fmac_f32_e32 v172, v56, v35
	v_mul_f32_e32 v42, v57, v56
	v_pk_mul_f32 v[44:45], v[174:175], v[44:45]
	v_fma_f32 v35, 0, v49, v201
	s_waitcnt lgkmcnt(1)
	v_pk_mul_f32 v[44:45], v[54:55], v[44:45]
	v_mov_b32_e32 v54, v198
	v_fma_f32 v43, v190, v172, v45
	v_pk_mul_f32 v[46:47], v[190:191], v[42:43]
	v_pk_mov_b32 v[50:51], v[190:191], v[44:45] op_sel:[1,0]
	v_mov_b32_e32 v55, v62
	v_pk_fma_f32 v[44:45], v[190:191], v[42:43], v[50:51]
	v_pk_mul_f32 v[46:47], v[50:51], v[46:47]
	v_pk_fma_f32 v[50:51], v[38:39], v[38:39], 1.0 op_sel_hi:[1,1,0] neg_lo:[1,0,0] neg_hi:[1,0,0]
	v_pk_fma_f32 v[54:55], v[54:55], v[54:55], 1.0 op_sel_hi:[1,1,0] neg_lo:[1,0,0] neg_hi:[1,0,0]
	v_sqrt_f32_e32 v52, v51
	v_sqrt_f32_e32 v53, v50
	v_sqrt_f32_e32 v54, v54
	v_sqrt_f32_e32 v55, v55
	v_fmac_f32_e32 v200, v48, v35
	v_pk_mul_f32 v[50:51], v[58:59], v[52:53]
	v_pk_fma_f32 v[52:53], v[194:195], v[194:195], 1.0 op_sel_hi:[1,1,0] neg_lo:[1,0,0] neg_hi:[1,0,0]
	s_waitcnt lgkmcnt(0)
	v_pk_mul_f32 v[56:57], v[188:189], v[50:51]
	v_sqrt_f32_e32 v52, v52
	v_sqrt_f32_e32 v53, v53
	v_mul_f32_e32 v48, v49, v48
	v_mov_b32_e32 v49, v194
	v_pk_mul_f32 v[48:49], v[62:63], v[48:49]
	v_pk_mul_f32 v[50:51], v[60:61], v[52:53]
	v_pk_mul_f32 v[60:61], v[198:199], v[48:49]
	v_pk_mul_f32 v[52:53], v[192:193], v[50:51]
	v_pk_mul_f32 v[50:51], v[64:65], v[54:55]
	v_fma_f32 v35, 0, v63, v53
	v_fmac_f32_e32 v52, v194, v35
	v_pk_mul_f32 v[50:51], v[196:197], v[50:51]
	v_fma_f32 v53, v38, v52, v57
	v_mov_b32_e32 v52, v49
	v_pk_mul_f32 v[54:55], v[38:39], v[52:53]
	v_pk_mov_b32 v[48:49], v[38:39], v[56:57] op_sel:[1,0]
	v_fma_f32 v35, v62, v200, v51
	v_pk_fma_f32 v[56:57], v[38:39], v[52:53], v[48:49]
	v_pk_mul_f32 v[52:53], v[48:49], v[54:55]
	ds_bpermute_b32 v38, v155, v60
	v_fmac_f32_e32 v50, v198, v35
	ds_bpermute_b32 v37, v155, v41
	ds_bpermute_b32 v36, v155, v34
	ds_bpermute_b32 v42, v155, v46
	ds_bpermute_b32 v43, v155, v45
	ds_bpermute_b32 v54, v155, v52
	ds_bpermute_b32 v55, v155, v57
	ds_bpermute_b32 v35, v155, v50
	v_mov_b32_e32 v53, v57
	s_waitcnt lgkmcnt(7)
	v_pk_mul_f32 v[58:59], v[38:39], v[60:61]
	s_and_saveexec_b64 s[6:7], s[0:1]
	s_xor_b64 s[6:7], exec, s[6:7]
	s_cbranch_execz .LBB0_1413
	s_waitcnt lgkmcnt(0)
	v_fmac_f32_e32 v35, 0, v38
	v_fmac_f32_e32 v50, v60, v35
	v_mov_b32_e32 v39, v55
	v_fmac_f32_e32 v39, v50, v54
	v_mov_b32_e32 v38, v54
	v_pk_mul_f32 v[50:51], v[58:59], v[54:55]
	v_pk_fma_f32 v[48:49], v[58:59], v[38:39], v[52:53]
	s_nop 0
	v_mul_f32_e32 v48, v52, v50

; template <bool FINAL, int z> __device__ __forceinline__ void rglru_blocks(LAS unsigned char* XCB, LAS float* XCF, LAS float* HS, const bf16x8 (&wa)[8], const bf16x8 (&wx)[8],
;         float ba, float bxx, float sp8, int r, int hh, int chl, float& st, float& CA, float& CB) {
;     ...
;         for (int bi = 0; bi < 2; ++bi) { const int tb = z ? 1 - bi : bi;
;             if (z == 1 && bi == 0) __builtin_amdgcn_s_sleep(8);
;             f32x16 ya, yx;
; #pragma unroll
;             for (int i = 0; i < 16; ++i) { ya[i] = ba; yx[i] = bxx; }
; #pragma unroll
;             for (int s = 0; s < 8; ++s) { const bf16x8 af = *(const LAS bf16x8*)(XCB + (32 * tb + r) * 272 + (16 * s + 8 * hh) * 2);
;                 ya = __builtin_amdgcn_mfma_f32_32x32x16_bf16(af, wa[s], ya, 0, 0, 0); yx = __builtin_amdgcn_mfma_f32_32x32x16_bf16(af, wx[s], yx, 0, 0, 0); }
;             float av[16], bv[16];
; #pragma unroll
;             for (int i = 0; i < 16; i += 2) {
;                 typedef float f2 __attribute__((ext_vector_type(2)));
;                 const f2 xc = {XCF[(32 * tb + crow(i, hh)) * 128 + chl], XCF[(32 * tb + crow(i + 1, hh)) * 128 + chl]};
;                 const f2 ta = (f2){ya[i], ya[i + 1]} * -1.4426950408889634f, tx = (f2){yx[i], yx[i + 1]} * -1.4426950408889634f;
;                 f2 ea, ex; ea.x = __builtin_amdgcn_exp2f(ta.x); ea.y = __builtin_amdgcn_exp2f(ta.y); ex.x = __builtin_amdgcn_exp2f(tx.x); ex.y = __builtin_amdgcn_exp2f(tx.y);
;                 const f2 da = ea + 1.0f, dx = ex + 1.0f;
;                 f2 rg, ig; rg.x = __builtin_amdgcn_rcpf(da.x); rg.y = __builtin_amdgcn_rcpf(da.y); ig.x = __builtin_amdgcn_rcpf(dx.x); ig.y = __builtin_amdgcn_rcpf(dx.y);
;                 const f2 la = rg * sp8; f2 a; a.x = __builtin_amdgcn_exp2f(la.x); a.y = __builtin_amdgcn_exp2f(la.y);
;                 const f2 om = a * -a + 1.0f; f2 sq; sq.x = __builtin_amdgcn_sqrtf(om.x); sq.y = __builtin_amdgcn_sqrtf(om.y);
;                 const f2 b = sq * ig * xc;
; template <bool FINAL> __device__ __forceinline__ void rglru_pass(Frame& F) {
;     ...
;         if (FINAL) {
; #pragma unroll
;             for (int it = 0; it < 2; ++it) { const int id = F.tid + 512 * it; gq[it] = *(const GAS v4u*)(Z1 + (size_t)(row0 + (id >> 4)) * 4096 + h * 128 + (id & 15) * 8); } }
;         float st = 0.f, CA = 1.f, CB = 0.f;
;         if (FINAL) st = CL[((c - cg) / ncg) * 256 + z * 128 + chl];
.LBB0_1603:
	v_add_u32_e32 v192, s15, v174
	v_ashrrev_i32_e32 v193, 31, v192
	v_add_u32_e32 v190, s15, v176
	v_lshlrev_b64 v[34:35], 13, v[192:193]
	v_ashrrev_i32_e32 v191, 31, v190
	v_lshl_add_u64 v[34:35], v[188:189], 0, v[34:35]
	v_lshlrev_b64 v[36:37], 13, v[190:191]
	v_lshl_add_u64 v[36:37], v[188:189], 0, v[36:37]
	global_load_dwordx4 v[168:171], v[34:35], off
	global_load_dwordx4 v[164:167], v[36:37], off
	s_abs_i32 s5, s22
	s_mul_hi_u32 s23, s5, s16
	s_mul_i32 s24, s23, s13
	s_ashr_i32 s4, s22, 31
	s_sub_i32 s5, s5, s24
	s_xor_b32 s4, s4, s14
	s_add_i32 s24, s23, 1
	s_sub_i32 s25, s5, s13
	s_cmp_ge_u32 s5, s13
	s_cselect_b32 s23, s24, s23
	s_cselect_b32 s5, s25, s5
	s_add_i32 s24, s23, 1
	s_cmp_ge_u32 s5, s13
	s_cselect_b32 s5, s24, s23
	s_xor_b32 s5, s5, s4
	s_sub_i32 s4, s5, s4
	v_lshl_add_u32 v34, s4, 10, v1
	ds_read_b32 v209, v34
	v_and_b32_e32 v35, 64, v203
	v_xor_b32_e32 v34, 32, v203
	v_add_u32_e32 v35, 64, v35
	v_cmp_lt_i32_e32 vcc, v34, v35
	s_mov_b64 s[4:5], -1
	s_nop 0
	v_cndmask_b32_e32 v34, v203, v34, vcc
	v_lshlrev_b32_e32 v159, 2, v34
	s_and_b64 vcc, exec, s[8:9]
	s_cbranch_vccz .LBB0_1605
	s_sleep 24
	ds_read_b128 v[210:213], v208 offset:8704
	ds_read_b128 v[214:217], v208 offset:8736
	s_mov_b64 s[4:5], 0
	s_waitcnt lgkmcnt(1)
	v_mfma_f32_32x32x16_bf16 v[50:65], v[210:213], v[66:69], v[2:17]
	v_mfma_f32_32x32x16_bf16 v[34:49], v[210:213], v[98:101], v[18:33]
	s_waitcnt lgkmcnt(0)
	v_mfma_f32_32x32x16_bf16 v[50:65], v[214:217], v[70:73], v[50:65]
	v_mfma_f32_32x32x16_bf16 v[34:49], v[214:217], v[102:105], v[34:49]
	ds_read_b128 v[210:213], v208 offset:8768
	ds_read_b128 v[214:217], v208 offset:8800
	s_waitcnt lgkmcnt(1)
	v_mfma_f32_32x32x16_bf16 v[50:65], v[210:213], v[74:77], v[50:65]
	v_mfma_f32_32x32x16_bf16 v[34:49], v[210:213], v[106:109], v[34:49]
	s_waitcnt lgkmcnt(0)
	v_mfma_f32_32x32x16_bf16 v[50:65], v[214:217], v[78:81], v[50:65]
	v_mfma_f32_32x32x16_bf16 v[34:49], v[214:217], v[110:113], v[34:49]
	ds_read_b128 v[210:213], v208 offset:8832
	ds_read_b128 v[214:217], v208 offset:8864
	s_waitcnt lgkmcnt(1)
	v_mfma_f32_32x32x16_bf16 v[50:65], v[210:213], v[82:85], v[50:65]
	v_mfma_f32_32x32x16_bf16 v[34:49], v[210:213], v[114:117], v[34:49]
	s_waitcnt lgkmcnt(0)
	v_mfma_f32_32x32x16_bf16 v[50:65], v[214:217], v[86:89], v[50:65]
	v_mfma_f32_32x32x16_bf16 v[34:49], v[214:217], v[118:121], v[34:49]
	ds_read_b128 v[210:213], v208 offset:8896
	ds_read_b128 v[214:217], v208 offset:8928
	s_waitcnt lgkmcnt(1)
	v_mfma_f32_32x32x16_bf16 v[50:65], v[210:213], v[90:93], v[50:65]
	s_waitcnt lgkmcnt(0)
	v_mfma_f32_32x32x16_bf16 v[50:65], v[214:217], v[94:97], v[50:65]
	v_mfma_f32_32x32x16_bf16 v[34:49], v[210:213], v[122:125], v[34:49]
	s_nop 10
	v_mul_f32_e64 v50, v50, s12
	v_mul_f32_e64 v51, v51, s12
	v_mul_f32_e64 v54, v54, s12
	v_mul_f32_e64 v55, v55, s12
	v_exp_f32_e32 v50, v50
	v_exp_f32_e32 v51, v51
	v_pk_mul_f32 v[52:53], v[52:53], s[12:13] op_sel_hi:[1,0]
	v_exp_f32_e32 v54, v54
	v_exp_f32_e32 v55, v55
	v_mfma_f32_32x32x16_bf16 v[34:49], v[214:217], v[126:129], v[34:49]
	v_add_f32_e64 v50, v50, 1.0
	v_add_f32_e64 v51, v51, 1.0
	v_exp_f32_e32 v52, v52
	v_rcp_f32_e32 v50, v50
	v_rcp_f32_e32 v51, v51
	v_exp_f32_e32 v53, v53
	v_pk_add_f32 v[54:55], v[54:55], 1.0 op_sel_hi:[1,0]
	ds_read2st64_b32 v[210:211], v175 offset0:132 offset1:134
	s_nop 3
	v_pk_mul_f32 v[34:35], v[34:35], s[12:13] op_sel_hi:[1,0]
	v_pk_add_f32 v[52:53], v[52:53], 1.0 op_sel_hi:[1,0]
	v_exp_f32_e32 v212, v34
	v_exp_f32_e32 v213, v35
	v_pk_mul_f32 v[34:35], v[182:183], v[50:51]
	v_rcp_f32_e32 v54, v54
	v_exp_f32_e32 v34, v34
	v_exp_f32_e32 v35, v35
	v_pk_add_f32 v[50:51], v[212:213], 1.0 op_sel_hi:[1,0]
	v_rcp_f32_e32 v55, v55
	v_rcp_f32_e32 v50, v50
	v_pk_fma_f32 v[212:213], v[34:35], v[34:35], 1.0 op_sel_hi:[1,1,0] neg_lo:[1,0,0] neg_hi:[1,0,0]
	v_rcp_f32_e32 v51, v51
	v_sqrt_f32_e32 v212, v212
	v_sqrt_f32_e32 v213, v213
	v_rcp_f32_e32 v52, v52
	v_rcp_f32_e32 v53, v53
	v_pk_mul_f32 v[38:39], v[38:39], s[12:13] op_sel_hi:[1,0]
	v_pk_mul_f32 v[50:51], v[50:51], v[212:213]
	v_pk_mul_f32 v[36:37], v[36:37], s[12:13] op_sel_hi:[1,0]
	v_exp_f32_e32 v214, v38
	v_exp_f32_e32 v215, v39
	v_pk_mul_f32 v[38:39], v[182:183], v[54:55]
	s_waitcnt lgkmcnt(0)
	v_pk_mul_f32 v[50:51], v[210:211], v[50:51]
	v_exp_f32_e32 v210, v36
	v_exp_f32_e32 v211, v37
	v_pk_mul_f32 v[36:37], v[182:183], v[52:53]
	v_exp_f32_e32 v38, v38
	v_exp_f32_e32 v39, v39
	v_exp_f32_e32 v36, v36
	v_exp_f32_e32 v37, v37
	v_pk_add_f32 v[54:55], v[214:215], 1.0 op_sel_hi:[1,0]
	v_pk_add_f32 v[52:53], v[210:211], 1.0 op_sel_hi:[1,0]
	v_rcp_f32_e32 v214, v54
	v_rcp_f32_e32 v215, v55
	v_pk_fma_f32 v[54:55], v[38:39], v[38:39], 1.0 op_sel_hi:[1,1,0] neg_lo:[1,0,0] neg_hi:[1,0,0]
	v_pk_fma_f32 v[210:211], v[36:37], v[36:37], 1.0 op_sel_hi:[1,1,0] neg_lo:[1,0,0] neg_hi:[1,0,0]
	v_sqrt_f32_e32 v216, v54
	v_sqrt_f32_e32 v217, v55
	v_pk_mul_f32 v[54:55], v[56:57], s[12:13] op_sel_hi:[1,0]
	v_rcp_f32_e32 v52, v52
	v_rcp_f32_e32 v53, v53
	v_sqrt_f32_e32 v210, v210
	v_sqrt_f32_e32 v211, v211
	v_exp_f32_e32 v56, v54
	v_exp_f32_e32 v57, v55
	ds_read2st64_b32 v[212:213], v175 offset0:136 offset1:138
	v_pk_mul_f32 v[58:59], v[58:59], s[12:13] op_sel_hi:[1,0]
	v_pk_mul_f32 v[52:53], v[52:53], v[210:211]
	ds_read2st64_b32 v[210:211], v175 offset0:148 offset1:150
	v_pk_add_f32 v[56:57], v[56:57], 1.0 op_sel_hi:[1,0]
	v_exp_f32_e32 v58, v58
	v_exp_f32_e32 v59, v59
	v_rcp_f32_e32 v56, v56
	v_rcp_f32_e32 v57, v57
	s_waitcnt lgkmcnt(1)
	v_pk_mul_f32 v[54:55], v[212:213], v[52:53]
	v_pk_mul_f32 v[52:53], v[214:215], v[216:217]
	v_pk_mul_f32 v[40:41], v[40:41], s[12:13] op_sel_hi:[1,0]
	v_pk_add_f32 v[58:59], v[58:59], 1.0 op_sel_hi:[1,0]
	s_waitcnt lgkmcnt(0)
; template <bool FINAL, int z> __device__ __forceinline__ void rglru_blocks(LAS unsigned char* XCB, LAS float* XCF, LAS float* HS, const bf16x8 (&wa)[8], const bf16x8 (&wx)[8],
;         float ba, float bxx, float sp8, int r, int hh, int chl, float& st, float& CA, float& CB) {
;     ...
;                 const f2 ta = (f2){ya[i], ya[i + 1]} * -1.4426950408889634f, tx = (f2){yx[i], yx[i + 1]} * -1.4426950408889634f;
;                 f2 ea, ex; ea.x = __builtin_amdgcn_exp2f(ta.x); ea.y = __builtin_amdgcn_exp2f(ta.y); ex.x = __builtin_amdgcn_exp2f(tx.x); ex.y = __builtin_amdgcn_exp2f(tx.y);
;                 const f2 da = ea + 1.0f, dx = ex + 1.0f;
;                 f2 rg, ig; rg.x = __builtin_amdgcn_rcpf(da.x); rg.y = __builtin_amdgcn_rcpf(da.y); ig.x = __builtin_amdgcn_rcpf(dx.x); ig.y = __builtin_amdgcn_rcpf(dx.y);
;                 const f2 la = rg * sp8; f2 a; a.x = __builtin_amdgcn_exp2f(la.x); a.y = __builtin_amdgcn_exp2f(la.y);
;                 const f2 om = a * -a + 1.0f; f2 sq; sq.x = __builtin_amdgcn_sqrtf(om.x); sq.y = __builtin_amdgcn_sqrtf(om.y);
;                 const f2 b = sq * ig * xc;
;                 av[i] = a.x; av[i + 1] = a.y; bv[i] = b.x; bv[i + 1] = b.y; }
;             float Ag[4], Bg[4], Ap[4], Bp[4];
; #pragma unroll
;             for (int g = 0; g < 4; ++g) { float A = 1.f, B = 0.f;
; #pragma unroll
;                 for (int k = 0; k < 4; ++k) { const int kk = z ? 3 - k : k; B = B * av[4 * g + kk] + bv[4 * g + kk]; A *= av[4 * g + kk]; }
;                 Ag[g] = A; Bg[g] = B; Ap[g] = __shfl_xor(A, 32); Bp[g] = __shfl_xor(B, 32); }
;             float ent[4]; float cur = st;
; #pragma unroll
;             for (int gi = 0; gi < 4; ++gi) { const int g = z ? 3 - gi : gi;
;                 const bool own_first = z ? (hh == 1) : (hh == 0);
;                 if (own_first) { ent[g] = cur; cur = Ag[g] * cur + Bg[g]; CB = Ag[g] * CB + Bg[g]; CA *= Ag[g]; cur = Ap[g] * cur + Bp[g]; CB = Ap[g] * CB + Bp[g]; CA *= Ap[g]; }
;                 else { cur = Ap[g] * cur + Bp[g]; CB = Ap[g] * CB + Bp[g]; CA *= Ap[g]; ent[g] = cur; cur = Ag[g] * cur + Bg[g]; CB = Ag[g] * CB + Bg[g]; CA *= Ag[g]; } }
	v_pk_mul_f32 v[52:53], v[210:211], v[52:53]
	v_exp_f32_e32 v210, v40
	v_exp_f32_e32 v211, v41
	v_pk_mul_f32 v[40:41], v[182:183], v[56:57]
	v_rcp_f32_e32 v58, v58
	v_rcp_f32_e32 v59, v59
	v_pk_mul_f32 v[60:61], v[60:61], s[12:13] op_sel_hi:[1,0]
	v_exp_f32_e32 v40, v40
	v_exp_f32_e32 v41, v41
	v_exp_f32_e32 v60, v60
	v_exp_f32_e32 v61, v61
	v_pk_mul_f32 v[64:65], v[64:65], s[12:13] op_sel_hi:[1,0]
	v_pk_mul_f32 v[42:43], v[42:43], s[12:13] op_sel_hi:[1,0]
	v_exp_f32_e32 v64, v64
	v_exp_f32_e32 v65, v65
	v_exp_f32_e32 v214, v42
	v_exp_f32_e32 v215, v43
	v_pk_mul_f32 v[42:43], v[182:183], v[58:59]
	v_pk_mul_f32 v[62:63], v[62:63], s[12:13] op_sel_hi:[1,0]
	v_pk_add_f32 v[56:57], v[210:211], 1.0 op_sel_hi:[1,0]
	v_pk_fma_f32 v[210:211], v[40:41], v[40:41], 1.0 op_sel_hi:[1,1,0] neg_lo:[1,0,0] neg_hi:[1,0,0]
	v_exp_f32_e32 v42, v42
	v_exp_f32_e32 v43, v43
	v_pk_add_f32 v[60:61], v[60:61], 1.0 op_sel_hi:[1,0]
	v_exp_f32_e32 v62, v62
	v_exp_f32_e32 v63, v63
	v_rcp_f32_e32 v56, v56
	v_rcp_f32_e32 v57, v57
	v_sqrt_f32_e32 v210, v210
	v_sqrt_f32_e32 v211, v211
	v_rcp_f32_e32 v60, v60
	v_rcp_f32_e32 v61, v61
	v_pk_add_f32 v[64:65], v[64:65], 1.0 op_sel_hi:[1,0]
	v_pk_add_f32 v[58:59], v[214:215], 1.0 op_sel_hi:[1,0]
	v_rcp_f32_e32 v64, v64
	v_rcp_f32_e32 v65, v65
	v_pk_fma_f32 v[214:215], v[42:43], v[42:43], 1.0 op_sel_hi:[1,1,0] neg_lo:[1,0,0] neg_hi:[1,0,0]
	v_pk_add_f32 v[62:63], v[62:63], 1.0 op_sel_hi:[1,0]
	v_pk_mul_f32 v[56:57], v[56:57], v[210:211]
	ds_read2st64_b32 v[210:211], v175 offset0:164 offset1:166
	v_rcp_f32_e32 v58, v58
	v_rcp_f32_e32 v59, v59
	v_sqrt_f32_e32 v214, v214
	v_sqrt_f32_e32 v215, v215
	v_pk_mul_f32 v[44:45], v[44:45], s[12:13] op_sel_hi:[1,0]
	v_pk_mul_f32 v[60:61], v[182:183], v[60:61]
	v_rcp_f32_e32 v62, v62
	v_rcp_f32_e32 v63, v63
	v_exp_f32_e32 v44, v44
	v_exp_f32_e32 v45, v45
	v_exp_f32_e32 v60, v60
	v_exp_f32_e32 v61, v61
	v_pk_mul_f32 v[48:49], v[48:49], s[12:13] op_sel_hi:[1,0]
	v_pk_mul_f32 v[64:65], v[182:183], v[64:65]
	v_exp_f32_e32 v48, v48
	v_exp_f32_e32 v49, v49
	v_exp_f32_e32 v64, v64
	v_exp_f32_e32 v65, v65
	v_pk_mul_f32 v[58:59], v[58:59], v[214:215]
	v_pk_mul_f32 v[46:47], v[46:47], s[12:13] op_sel_hi:[1,0]
	v_pk_mul_f32 v[62:63], v[182:183], v[62:63]
	s_waitcnt lgkmcnt(0)
	v_pk_mul_f32 v[58:59], v[210:211], v[58:59]
	v_pk_add_f32 v[44:45], v[44:45], 1.0 op_sel_hi:[1,0]
	v_pk_fma_f32 v[210:211], v[60:61], v[60:61], 1.0 op_sel_hi:[1,1,0] neg_lo:[1,0,0] neg_hi:[1,0,0]
	v_exp_f32_e32 v46, v46
	v_exp_f32_e32 v47, v47
	v_exp_f32_e32 v62, v62
	v_exp_f32_e32 v63, v63
	v_rcp_f32_e32 v44, v44
	v_rcp_f32_e32 v45, v45
	v_sqrt_f32_e32 v210, v210
	v_sqrt_f32_e32 v211, v211
	ds_read2st64_b32 v[212:213], v175 offset0:152 offset1:154
	v_pk_add_f32 v[48:49], v[48:49], 1.0 op_sel_hi:[1,0]
	v_pk_fma_f32 v[218:219], v[64:65], v[64:65], 1.0 op_sel_hi:[1,1,0] neg_lo:[1,0,0] neg_hi:[1,0,0]
	ds_read2st64_b32 v[216:217], v175 offset0:184 offset1:186
	v_rcp_f32_e32 v48, v48
	v_rcp_f32_e32 v49, v49
	v_sqrt_f32_e32 v218, v218
	v_sqrt_f32_e32 v219, v219
	v_pk_add_f32 v[46:47], v[46:47], 1.0 op_sel_hi:[1,0]
	v_pk_fma_f32 v[214:215], v[62:63], v[62:63], 1.0 op_sel_hi:[1,1,0] neg_lo:[1,0,0] neg_hi:[1,0,0]
	v_pk_mul_f32 v[44:45], v[44:45], v[210:211]
	ds_read2st64_b32 v[210:211], v175 offset0:180 offset1:182
	v_rcp_f32_e32 v46, v46
	v_rcp_f32_e32 v47, v47
	v_sqrt_f32_e32 v214, v214
	v_sqrt_f32_e32 v215, v215
	s_waitcnt lgkmcnt(2)
	v_pk_mul_f32 v[56:57], v[212:213], v[56:57]
	ds_read2st64_b32 v[212:213], v175 offset0:168 offset1:170
	v_pk_mul_f32 v[48:49], v[48:49], v[218:219]
	v_pk_mul_f32 v[46:47], v[46:47], v[214:215]
	s_waitcnt lgkmcnt(2)
	v_pk_mul_f32 v[48:49], v[216:217], v[48:49]
	s_waitcnt lgkmcnt(1)
	v_pk_mul_f32 v[46:47], v[210:211], v[46:47]
	v_fma_f32 v218, 0, v65, v49
	v_fma_f32 v218, v64, v218, v48
	v_mul_f32_e32 v219, v65, v64
	v_fma_f32 v218, v63, v218, v47
	v_mul_f32_e32 v219, v63, v219
	s_waitcnt lgkmcnt(0)
	v_pk_mul_f32 v[44:45], v[212:213], v[44:45]
	v_fma_f32 v218, v62, v218, v46
	v_mul_f32_e32 v219, v62, v219
	v_fma_f32 v216, 0, v61, v45
	ds_bpermute_b32 v222, v159, v219
	ds_bpermute_b32 v223, v159, v218
	v_fma_f32 v210, 0, v37, v55
	v_fma_f32 v216, v60, v216, v44
	v_mul_f32_e32 v217, v61, v60
	v_fma_f32 v210, v36, v210, v54
	v_fma_f32 v216, v43, v216, v59
	v_mul_f32_e32 v217, v43, v217
	v_fma_f32 v210, v35, v210, v51
	v_fma_f32 v216, v42, v216, v58
	v_mul_f32_e32 v217, v42, v217
	v_fma_f32 v220, v34, v210, v50
	v_fma_f32 v210, 0, v41, v57
	ds_bpermute_b32 v224, v159, v217
	ds_bpermute_b32 v225, v159, v216
	v_fma_f32 v226, v209, v219, v218
	v_fma_f32 v210, v40, v210, v56
	v_mul_f32_e32 v213, v41, v40
	s_waitcnt lgkmcnt(2)
	v_fma_f32 v226, v226, v222, v223
	v_fmac_f32_e32 v223, v209, v222
	v_fma_f32 v210, v39, v210, v53
	v_mul_f32_e32 v213, v39, v213
	v_fmac_f32_e32 v218, v219, v223
	v_fma_f32 v210, v38, v210, v52
	v_mul_f32_e32 v213, v38, v213
	v_cndmask_b32_e64 v218, v218, v226, s[0:1]
	ds_bpermute_b32 v214, v159, v213
	ds_bpermute_b32 v215, v159, v210
	v_fma_f32 v222, v217, v218, v216
	v_mul_f32_e32 v211, v37, v36
	s_waitcnt lgkmcnt(2)
	v_fma_f32 v222, v222, v224, v225
	v_fmac_f32_e32 v225, v218, v224
	v_mul_f32_e32 v211, v35, v211
	v_fmac_f32_e32 v216, v217, v225
	v_mul_f32_e32 v211, v34, v211
	v_cndmask_b32_e64 v216, v216, v222, s[0:1]
	ds_bpermute_b32 v212, v159, v211
	ds_bpermute_b32 v221, v159, v220
	v_fma_f32 v218, v213, v216, v210
	s_waitcnt lgkmcnt(2)
	v_fma_f32 v218, v218, v214, v215
	v_fmac_f32_e32 v215, v216, v214
	v_fmac_f32_e32 v210, v213, v215
	v_cndmask_b32_e64 v214, v210, v218, s[0:1]
	v_fma_f32 v210, v211, v214, v220
	s_waitcnt lgkmcnt(0)
; #define LAS __attribute__((address_space(3)))
; __device__ __forceinline__ int crow(int r, int hh) { return (r & 3) + 8 * (r >> 2) + 4 * hh; }
; template <bool FINAL, int z> __device__ __forceinline__ void rglru_blocks(LAS unsigned char* XCB, LAS float* XCF, LAS float* HS, const bf16x8 (&wa)[8], const bf16x8 (&wx)[8],
;         float ba, float bxx, float sp8, int r, int hh, int chl, float& st, float& CA, float& CB) {
;     ...
;             for (int s = 0; s < 8; ++s) { const bf16x8 af = *(const LAS bf16x8*)(XCB + (32 * tb + r) * 272 + (16 * s + 8 * hh) * 2);
;                 ya = __builtin_amdgcn_mfma_f32_32x32x16_bf16(af, wa[s], ya, 0, 0, 0); yx = __builtin_amdgcn_mfma_f32_32x32x16_bf16(af, wx[s], yx, 0, 0, 0); }
;             float av[16], bv[16];
; #pragma unroll
;             for (int i = 0; i < 16; i += 2) {
;                 typedef float f2 __attribute__((ext_vector_type(2)));
;                 const f2 xc = {XCF[(32 * tb + crow(i, hh)) * 128 + chl], XCF[(32 * tb + crow(i + 1, hh)) * 128 + chl]};
;                 const f2 ta = (f2){ya[i], ya[i + 1]} * -1.4426950408889634f, tx = (f2){yx[i], yx[i + 1]} * -1.4426950408889634f;
;     ...
;             for (int g = 0; g < 4; ++g) { float A = 1.f, B = 0.f;
; #pragma unroll
;                 for (int k = 0; k < 4; ++k) { const int kk = z ? 3 - k : k; B = B * av[4 * g + kk] + bv[4 * g + kk]; A *= av[4 * g + kk]; }
;                 Ag[g] = A; Bg[g] = B; Ap[g] = __shfl_xor(A, 32); Bp[g] = __shfl_xor(B, 32); }
;             float ent[4]; float cur = st;
; #pragma unroll
;             for (int gi = 0; gi < 4; ++gi) { const int g = z ? 3 - gi : gi;
;                 const bool own_first = z ? (hh == 1) : (hh == 0);
;                 if (own_first) { ent[g] = cur; cur = Ag[g] * cur + Bg[g]; CB = Ag[g] * CB + Bg[g]; CA *= Ag[g]; cur = Ap[g] * cur + Bp[g]; CB = Ap[g] * CB + Bp[g]; CA *= Ap[g]; }
;                 else { cur = Ap[g] * cur + Bp[g]; CB = Ap[g] * CB + Bp[g]; CA *= Ap[g]; ent[g] = cur; cur = Ag[g] * cur + Bg[g]; CB = Ag[g] * CB + Bg[g]; CA *= Ag[g]; } }
;             st = cur;
;             if (FINAL) {
; #pragma unroll
;                 for (int g = 0; g < 4; ++g) { float hc = ent[g];
; #pragma unroll
;                     for (int k = 0; k < 4; ++k) { const int kk = z ? 3 - k : k; hc = av[4 * g + kk] * hc + bv[4 * g + kk];
;                         HS[(z * 64 + 32 * tb + 8 * g + 4 * hh + kk) * 128 + chl] = hc; } } }
	v_fma_f32 v210, v210, v212, v221
	v_fmac_f32_e32 v221, v214, v212
	v_cndmask_b32_e64 v212, v221, v218, s[0:1]
	v_fma_f32 v37, v37, v212, v55
	v_fmac_f32_e32 v54, v36, v37
	v_cndmask_b32_e64 v213, v215, v222, s[0:1]
	v_fma_f32 v35, v35, v54, v51
	v_fmac_f32_e32 v50, v34, v35
	v_fma_f32 v34, v41, v213, v57
	v_fmac_f32_e32 v56, v40, v34
	ds_write2st64_b32 v177, v56, v34 offset0:212 offset1:214
	v_fma_f32 v34, v39, v56, v53
	v_cndmask_b32_e64 v217, v225, v226, s[0:1]
	v_fmac_f32_e32 v52, v38, v34
	ds_write2st64_b32 v177, v52, v34 offset0:208 offset1:210
	v_fma_f32 v34, v61, v217, v45
	v_fmac_f32_e32 v44, v60, v34
	ds_write2st64_b32 v177, v44, v34 offset0:228 offset1:230
	v_fma_f32 v34, v43, v44, v59
	v_cndmask_b32_e64 v219, v223, v209, s[0:1]
	v_fmac_f32_e32 v58, v42, v34
	ds_write2st64_b32 v177, v58, v34 offset0:224 offset1:226
	v_fma_f32 v34, v65, v219, v49
	v_fmac_f32_e32 v48, v64, v34
	ds_write2st64_b32 v177, v48, v34 offset0:244 offset1:246
	v_fma_f32 v34, v63, v48, v47
	v_fmac_f32_e32 v46, v62, v34
	ds_write2st64_b32 v177, v54, v37 offset0:196 offset1:198
	ds_write2st64_b32 v177, v50, v35 offset0:192 offset1:194
	ds_write2st64_b32 v177, v46, v34 offset0:240 offset1:242
	ds_read_b128 v[212:215], v208
	ds_read_b128 v[216:219], v208 offset:32
	s_waitcnt lgkmcnt(1)
	v_mfma_f32_32x32x16_bf16 v[50:65], v[212:215], v[66:69], v[2:17]
	v_fmac_f32_e32 v220, v211, v221
	v_cndmask_b32_e64 v211, v220, v210, s[0:1]
	v_mfma_f32_32x32x16_bf16 v[34:49], v[212:215], v[98:101], v[18:33]
	s_waitcnt lgkmcnt(0)
	v_mfma_f32_32x32x16_bf16 v[50:65], v[216:219], v[70:73], v[50:65]
	v_mfma_f32_32x32x16_bf16 v[34:49], v[216:219], v[102:105], v[34:49]
	ds_read_b128 v[212:215], v208 offset:64
	ds_read_b128 v[216:219], v208 offset:96
	s_waitcnt lgkmcnt(1)
	v_mfma_f32_32x32x16_bf16 v[50:65], v[212:215], v[74:77], v[50:65]
	v_mfma_f32_32x32x16_bf16 v[34:49], v[212:215], v[106:109], v[34:49]
	s_waitcnt lgkmcnt(0)
	v_mfma_f32_32x32x16_bf16 v[50:65], v[216:219], v[78:81], v[50:65]
	v_mfma_f32_32x32x16_bf16 v[34:49], v[216:219], v[110:113], v[34:49]
	ds_read_b128 v[212:215], v208 offset:128
	ds_read_b128 v[216:219], v208 offset:160
	s_waitcnt lgkmcnt(1)
	v_mfma_f32_32x32x16_bf16 v[50:65], v[212:215], v[82:85], v[50:65]
	v_mfma_f32_32x32x16_bf16 v[34:49], v[212:215], v[114:117], v[34:49]
	s_waitcnt lgkmcnt(0)
	v_mfma_f32_32x32x16_bf16 v[50:65], v[216:219], v[86:89], v[50:65]
	v_mfma_f32_32x32x16_bf16 v[34:49], v[216:219], v[118:121], v[34:49]
	ds_read_b128 v[212:215], v208 offset:192
	ds_read_b128 v[216:219], v208 offset:224
	s_waitcnt lgkmcnt(1)
	v_mfma_f32_32x32x16_bf16 v[50:65], v[212:215], v[90:93], v[50:65]
	s_waitcnt lgkmcnt(0)
	v_mfma_f32_32x32x16_bf16 v[50:65], v[216:219], v[94:97], v[50:65]
	v_mfma_f32_32x32x16_bf16 v[34:49], v[212:215], v[122:125], v[34:49]
	s_nop 10
	v_mul_f32_e64 v50, v50, s12
	v_mul_f32_e64 v51, v51, s12
	v_mul_f32_e64 v54, v54, s12
	v_mul_f32_e64 v55, v55, s12
	v_exp_f32_e32 v50, v50
	v_exp_f32_e32 v51, v51
	v_pk_mul_f32 v[52:53], v[52:53], s[12:13] op_sel_hi:[1,0]
	v_exp_f32_e32 v54, v54
	v_exp_f32_e32 v55, v55
	v_mfma_f32_32x32x16_bf16 v[34:49], v[216:219], v[126:129], v[34:49]
	v_add_f32_e64 v50, v50, 1.0
	v_add_f32_e64 v51, v51, 1.0
	v_exp_f32_e32 v52, v52
	v_rcp_f32_e32 v50, v50
	v_rcp_f32_e32 v51, v51
	v_exp_f32_e32 v53, v53
	v_pk_add_f32 v[54:55], v[54:55], 1.0 op_sel_hi:[1,0]
	ds_read2st64_b32 v[212:213], v175 offset0:68 offset1:70
	s_nop 3
	v_pk_mul_f32 v[34:35], v[34:35], s[12:13] op_sel_hi:[1,0]
	v_pk_add_f32 v[52:53], v[52:53], 1.0 op_sel_hi:[1,0]
	v_exp_f32_e32 v214, v34
	v_exp_f32_e32 v215, v35
	v_pk_mul_f32 v[34:35], v[182:183], v[50:51]
	v_rcp_f32_e32 v54, v54
	v_exp_f32_e32 v34, v34
	v_exp_f32_e32 v35, v35
	v_pk_add_f32 v[50:51], v[214:215], 1.0 op_sel_hi:[1,0]
	v_rcp_f32_e32 v55, v55
	v_rcp_f32_e32 v50, v50
	v_pk_fma_f32 v[214:215], v[34:35], v[34:35], 1.0 op_sel_hi:[1,1,0] neg_lo:[1,0,0] neg_hi:[1,0,0]
	v_rcp_f32_e32 v51, v51
	v_sqrt_f32_e32 v214, v214
	v_sqrt_f32_e32 v215, v215
	v_rcp_f32_e32 v52, v52
	v_rcp_f32_e32 v53, v53
	v_pk_mul_f32 v[38:39], v[38:39], s[12:13] op_sel_hi:[1,0]
	v_pk_mul_f32 v[50:51], v[50:51], v[214:215]
	v_pk_mul_f32 v[36:37], v[36:37], s[12:13] op_sel_hi:[1,0]
	v_exp_f32_e32 v216, v38
	v_exp_f32_e32 v217, v39
	v_pk_mul_f32 v[38:39], v[182:183], v[54:55]
	s_waitcnt lgkmcnt(0)
	v_pk_mul_f32 v[50:51], v[212:213], v[50:51]
	v_exp_f32_e32 v212, v36
	v_exp_f32_e32 v213, v37
	v_pk_mul_f32 v[36:37], v[182:183], v[52:53]
	v_exp_f32_e32 v38, v38
	v_exp_f32_e32 v39, v39
	v_exp_f32_e32 v36, v36
	v_exp_f32_e32 v37, v37
	v_pk_add_f32 v[54:55], v[216:217], 1.0 op_sel_hi:[1,0]
	v_pk_add_f32 v[52:53], v[212:213], 1.0 op_sel_hi:[1,0]
	v_rcp_f32_e32 v216, v54
	v_rcp_f32_e32 v217, v55
	v_pk_fma_f32 v[54:55], v[38:39], v[38:39], 1.0 op_sel_hi:[1,1,0] neg_lo:[1,0,0] neg_hi:[1,0,0]
	v_pk_fma_f32 v[212:213], v[36:37], v[36:37], 1.0 op_sel_hi:[1,1,0] neg_lo:[1,0,0] neg_hi:[1,0,0]
	v_sqrt_f32_e32 v218, v54
	v_sqrt_f32_e32 v219, v55
	v_pk_mul_f32 v[54:55], v[56:57], s[12:13] op_sel_hi:[1,0]
	v_rcp_f32_e32 v52, v52
	v_rcp_f32_e32 v53, v53
	v_sqrt_f32_e32 v212, v212
	v_sqrt_f32_e32 v213, v213
	v_exp_f32_e32 v56, v54
	v_exp_f32_e32 v57, v55
	ds_read2st64_b32 v[214:215], v175 offset0:72 offset1:74
	v_pk_mul_f32 v[58:59], v[58:59], s[12:13] op_sel_hi:[1,0]
	v_pk_mul_f32 v[52:53], v[52:53], v[212:213]
	ds_read2st64_b32 v[212:213], v175 offset0:84 offset1:86
	v_pk_add_f32 v[56:57], v[56:57], 1.0 op_sel_hi:[1,0]
	v_exp_f32_e32 v58, v58
	v_exp_f32_e32 v59, v59
	v_rcp_f32_e32 v56, v56
	v_rcp_f32_e32 v57, v57
	s_waitcnt lgkmcnt(1)
; template <bool FINAL, int z> __device__ __forceinline__ void rglru_blocks(LAS unsigned char* XCB, LAS float* XCF, LAS float* HS, const bf16x8 (&wa)[8], const bf16x8 (&wx)[8],
;         float ba, float bxx, float sp8, int r, int hh, int chl, float& st, float& CA, float& CB) {
;     ...
;             for (int i = 0; i < 16; i += 2) {
;                 typedef float f2 __attribute__((ext_vector_type(2)));
;                 const f2 xc = {XCF[(32 * tb + crow(i, hh)) * 128 + chl], XCF[(32 * tb + crow(i + 1, hh)) * 128 + chl]};
;                 const f2 ta = (f2){ya[i], ya[i + 1]} * -1.4426950408889634f, tx = (f2){yx[i], yx[i + 1]} * -1.4426950408889634f;
;                 f2 ea, ex; ea.x = __builtin_amdgcn_exp2f(ta.x); ea.y = __builtin_amdgcn_exp2f(ta.y); ex.x = __builtin_amdgcn_exp2f(tx.x); ex.y = __builtin_amdgcn_exp2f(tx.y);
;                 const f2 da = ea + 1.0f, dx = ex + 1.0f;
;                 f2 rg, ig; rg.x = __builtin_amdgcn_rcpf(da.x); rg.y = __builtin_amdgcn_rcpf(da.y); ig.x = __builtin_amdgcn_rcpf(dx.x); ig.y = __builtin_amdgcn_rcpf(dx.y);
;                 const f2 la = rg * sp8; f2 a; a.x = __builtin_amdgcn_exp2f(la.x); a.y = __builtin_amdgcn_exp2f(la.y);
;                 const f2 om = a * -a + 1.0f; f2 sq; sq.x = __builtin_amdgcn_sqrtf(om.x); sq.y = __builtin_amdgcn_sqrtf(om.y);
;                 const f2 b = sq * ig * xc;
;                 av[i] = a.x; av[i + 1] = a.y; bv[i] = b.x; bv[i + 1] = b.y; }
;             float Ag[4], Bg[4], Ap[4], Bp[4];
; #pragma unroll
;             for (int g = 0; g < 4; ++g) { float A = 1.f, B = 0.f;
; #pragma unroll
;                 for (int k = 0; k < 4; ++k) { const int kk = z ? 3 - k : k; B = B * av[4 * g + kk] + bv[4 * g + kk]; A *= av[4 * g + kk]; }
;                 Ag[g] = A; Bg[g] = B; Ap[g] = __shfl_xor(A, 32); Bp[g] = __shfl_xor(B, 32); }
;             float ent[4]; float cur = st;
; #pragma unroll
;             for (int gi = 0; gi < 4; ++gi) { const int g = z ? 3 - gi : gi;
;                 const bool own_first = z ? (hh == 1) : (hh == 0);
;                 if (own_first) { ent[g] = cur; cur = Ag[g] * cur + Bg[g]; CB = Ag[g] * CB + Bg[g]; CA *= Ag[g]; cur = Ap[g] * cur + Bp[g]; CB = Ap[g] * CB + Bp[g]; CA *= Ap[g]; }
;                 else { cur = Ap[g] * cur + Bp[g]; CB = Ap[g] * CB + Bp[g]; CA *= Ap[g]; ent[g] = cur; cur = Ag[g] * cur + Bg[g]; CB = Ag[g] * CB + Bg[g]; CA *= Ag[g]; } }
	v_pk_mul_f32 v[54:55], v[214:215], v[52:53]
	v_pk_mul_f32 v[52:53], v[216:217], v[218:219]
	v_pk_mul_f32 v[40:41], v[40:41], s[12:13] op_sel_hi:[1,0]
	v_pk_add_f32 v[58:59], v[58:59], 1.0 op_sel_hi:[1,0]
	s_waitcnt lgkmcnt(0)
	v_pk_mul_f32 v[52:53], v[212:213], v[52:53]
	v_exp_f32_e32 v212, v40
	v_exp_f32_e32 v213, v41
	v_pk_mul_f32 v[40:41], v[182:183], v[56:57]
	v_rcp_f32_e32 v58, v58
	v_rcp_f32_e32 v59, v59
	v_pk_mul_f32 v[60:61], v[60:61], s[12:13] op_sel_hi:[1,0]
	v_exp_f32_e32 v40, v40
	v_exp_f32_e32 v41, v41
	v_exp_f32_e32 v60, v60
	v_exp_f32_e32 v61, v61
	v_pk_mul_f32 v[64:65], v[64:65], s[12:13] op_sel_hi:[1,0]
	v_pk_mul_f32 v[42:43], v[42:43], s[12:13] op_sel_hi:[1,0]
	v_exp_f32_e32 v64, v64
	v_exp_f32_e32 v65, v65
	v_exp_f32_e32 v216, v42
	v_exp_f32_e32 v217, v43
	v_pk_mul_f32 v[42:43], v[182:183], v[58:59]
	v_pk_mul_f32 v[62:63], v[62:63], s[12:13] op_sel_hi:[1,0]
	v_pk_add_f32 v[56:57], v[212:213], 1.0 op_sel_hi:[1,0]
	v_pk_fma_f32 v[212:213], v[40:41], v[40:41], 1.0 op_sel_hi:[1,1,0] neg_lo:[1,0,0] neg_hi:[1,0,0]
	v_exp_f32_e32 v42, v42
	v_exp_f32_e32 v43, v43
	v_pk_add_f32 v[60:61], v[60:61], 1.0 op_sel_hi:[1,0]
	v_exp_f32_e32 v62, v62
	v_exp_f32_e32 v63, v63
	v_rcp_f32_e32 v56, v56
	v_rcp_f32_e32 v57, v57
	v_sqrt_f32_e32 v212, v212
	v_sqrt_f32_e32 v213, v213
	v_rcp_f32_e32 v60, v60
	v_rcp_f32_e32 v61, v61
	v_pk_add_f32 v[64:65], v[64:65], 1.0 op_sel_hi:[1,0]
	v_pk_add_f32 v[58:59], v[216:217], 1.0 op_sel_hi:[1,0]
	v_rcp_f32_e32 v64, v64
	v_rcp_f32_e32 v65, v65
	v_pk_fma_f32 v[216:217], v[42:43], v[42:43], 1.0 op_sel_hi:[1,1,0] neg_lo:[1,0,0] neg_hi:[1,0,0]
	v_pk_add_f32 v[62:63], v[62:63], 1.0 op_sel_hi:[1,0]
	v_pk_mul_f32 v[56:57], v[56:57], v[212:213]
	ds_read2st64_b32 v[212:213], v175 offset0:100 offset1:102
	v_rcp_f32_e32 v58, v58
	v_rcp_f32_e32 v59, v59
	v_sqrt_f32_e32 v216, v216
	v_sqrt_f32_e32 v217, v217
	v_pk_mul_f32 v[44:45], v[44:45], s[12:13] op_sel_hi:[1,0]
	v_pk_mul_f32 v[60:61], v[182:183], v[60:61]
	v_rcp_f32_e32 v62, v62
	v_rcp_f32_e32 v63, v63
	v_exp_f32_e32 v44, v44
	v_exp_f32_e32 v45, v45
	v_exp_f32_e32 v60, v60
	v_exp_f32_e32 v61, v61
	v_pk_mul_f32 v[48:49], v[48:49], s[12:13] op_sel_hi:[1,0]
	v_pk_mul_f32 v[64:65], v[182:183], v[64:65]
	v_exp_f32_e32 v48, v48
	v_exp_f32_e32 v49, v49
	v_exp_f32_e32 v64, v64
	v_exp_f32_e32 v65, v65
	v_pk_mul_f32 v[58:59], v[58:59], v[216:217]
	v_pk_mul_f32 v[46:47], v[46:47], s[12:13] op_sel_hi:[1,0]
	v_pk_mul_f32 v[62:63], v[182:183], v[62:63]
	s_waitcnt lgkmcnt(0)
	v_pk_mul_f32 v[58:59], v[212:213], v[58:59]
	v_pk_add_f32 v[44:45], v[44:45], 1.0 op_sel_hi:[1,0]
	v_pk_fma_f32 v[212:213], v[60:61], v[60:61], 1.0 op_sel_hi:[1,1,0] neg_lo:[1,0,0] neg_hi:[1,0,0]
	v_exp_f32_e32 v46, v46
	v_exp_f32_e32 v47, v47
	v_exp_f32_e32 v62, v62
	v_exp_f32_e32 v63, v63
	v_rcp_f32_e32 v44, v44
	v_rcp_f32_e32 v45, v45
	v_sqrt_f32_e32 v212, v212
	v_sqrt_f32_e32 v213, v213
	ds_read2st64_b32 v[214:215], v175 offset0:88 offset1:90
	v_pk_add_f32 v[48:49], v[48:49], 1.0 op_sel_hi:[1,0]
	v_pk_fma_f32 v[220:221], v[64:65], v[64:65], 1.0 op_sel_hi:[1,1,0] neg_lo:[1,0,0] neg_hi:[1,0,0]
	ds_read2st64_b32 v[218:219], v175 offset0:120 offset1:122
	v_rcp_f32_e32 v48, v48
	v_rcp_f32_e32 v49, v49
	v_sqrt_f32_e32 v220, v220
	v_sqrt_f32_e32 v221, v221
	v_pk_add_f32 v[46:47], v[46:47], 1.0 op_sel_hi:[1,0]
	v_pk_fma_f32 v[216:217], v[62:63], v[62:63], 1.0 op_sel_hi:[1,1,0] neg_lo:[1,0,0] neg_hi:[1,0,0]
	v_pk_mul_f32 v[44:45], v[44:45], v[212:213]
	ds_read2st64_b32 v[212:213], v175 offset0:116 offset1:118
	v_rcp_f32_e32 v46, v46
	v_rcp_f32_e32 v47, v47
	v_sqrt_f32_e32 v216, v216
	v_sqrt_f32_e32 v217, v217
	s_waitcnt lgkmcnt(2)
	v_pk_mul_f32 v[56:57], v[214:215], v[56:57]
	ds_read2st64_b32 v[214:215], v175 offset0:104 offset1:106
	v_pk_mul_f32 v[48:49], v[48:49], v[220:221]
	v_pk_mul_f32 v[46:47], v[46:47], v[216:217]
	s_waitcnt lgkmcnt(2)
	v_pk_mul_f32 v[48:49], v[218:219], v[48:49]
	s_waitcnt lgkmcnt(1)
	v_pk_mul_f32 v[46:47], v[212:213], v[46:47]
	v_fma_f32 v220, 0, v65, v49
	v_fma_f32 v220, v64, v220, v48
	v_mul_f32_e32 v221, v65, v64
	v_fma_f32 v220, v63, v220, v47
	v_mul_f32_e32 v221, v63, v221
	s_waitcnt lgkmcnt(0)
	v_pk_mul_f32 v[44:45], v[214:215], v[44:45]
	v_fma_f32 v220, v62, v220, v46
	v_mul_f32_e32 v221, v62, v221
	v_fma_f32 v218, 0, v61, v45
	ds_bpermute_b32 v222, v159, v221
	ds_bpermute_b32 v223, v159, v220
	v_fma_f32 v218, v60, v218, v44
	v_mul_f32_e32 v219, v61, v60
	v_fma_f32 v218, v43, v218, v59
	v_mul_f32_e32 v219, v43, v219
	v_fma_f32 v218, v42, v218, v58
	v_mul_f32_e32 v219, v42, v219
	v_fma_f32 v214, 0, v41, v57
	ds_bpermute_b32 v224, v159, v219
	ds_bpermute_b32 v225, v159, v218
	v_fma_f32 v226, v211, v221, v220
	v_fma_f32 v214, v40, v214, v56
	v_mul_f32_e32 v215, v41, v40
	s_waitcnt lgkmcnt(2)
	v_fma_f32 v226, v226, v222, v223
	v_fmac_f32_e32 v223, v211, v222
	v_fma_f32 v214, v39, v214, v53
	v_mul_f32_e32 v215, v39, v215
	v_fmac_f32_e32 v220, v221, v223
	v_fma_f32 v212, 0, v37, v55
	v_fma_f32 v214, v38, v214, v52
	v_mul_f32_e32 v215, v38, v215
	v_cndmask_b32_e64 v211, v220, v226, s[0:1]
	v_fma_f32 v212, v36, v212, v54
	v_mul_f32_e32 v213, v37, v36
	ds_bpermute_b32 v216, v159, v215
	ds_bpermute_b32 v217, v159, v214
	v_fma_f32 v220, v219, v211, v218
	v_fma_f32 v212, v35, v212, v51
	v_mul_f32_e32 v213, v35, v213
	s_waitcnt lgkmcnt(2)
	v_fma_f32 v220, v220, v224, v225
	v_fmac_f32_e32 v225, v211, v224
	v_fma_f32 v212, v34, v212, v50
	v_mul_f32_e32 v213, v34, v213
	v_fmac_f32_e32 v218, v219, v225
	ds_bpermute_b32 v213, v159, v213
	ds_bpermute_b32 v212, v159, v212
	v_cndmask_b32_e64 v218, v218, v220, s[0:1]
	v_fma_f32 v219, v215, v218, v214
	s_waitcnt lgkmcnt(2)
	v_fma_f32 v219, v219, v216, v217
	v_fmac_f32_e32 v217, v218, v216
	v_fmac_f32_e32 v214, v215, v217
	v_cndmask_b32_e64 v214, v214, v219, s[0:1]
	s_waitcnt lgkmcnt(0)
	v_fmac_f32_e32 v212, v214, v213
	v_cndmask_b32_e64 v212, v212, v219, s[0:1]
	v_fma_f32 v37, v37, v212, v55
	v_fmac_f32_e32 v54, v36, v37
	v_cndmask_b32_e64 v215, v217, v220, s[0:1]
	v_fma_f32 v35, v35, v54, v51
	v_fmac_f32_e32 v50, v34, v35
	v_fma_f32 v34, v41, v215, v57
	v_fmac_f32_e32 v56, v40, v34
	ds_write2st64_b32 v177, v56, v34 offset0:148 offset1:150
	v_fma_f32 v34, v39, v56, v53
	v_cndmask_b32_e64 v211, v225, v226, s[0:1]
	v_fmac_f32_e32 v52, v38, v34
	ds_write2st64_b32 v177, v52, v34 offset0:144 offset1:146
	v_fma_f32 v34, v61, v211, v45
	v_fmac_f32_e32 v44, v60, v34
	ds_write2st64_b32 v177, v44, v34 offset0:164 offset1:166
	v_fma_f32 v34, v43, v44, v59
	v_cndmask_b32_e64 v210, v223, v210, s[0:1]
	v_fmac_f32_e32 v58, v42, v34
	ds_write2st64_b32 v177, v58, v34 offset0:160 offset1:162
	v_fma_f32 v34, v65, v210, v49
	v_fmac_f32_e32 v48, v64, v34
	ds_write2st64_b32 v177, v48, v34 offset0:180 offset1:182
	v_fma_f32 v34, v63, v48, v47
	v_fmac_f32_e32 v46, v62, v34
	ds_write2st64_b32 v177, v54, v37 offset0:132 offset1:134
	ds_write2st64_b32 v177, v50, v35 offset0:128 offset1:130
	ds_write2st64_b32 v177, v46, v34 offset0:176 offset1:178
